# speedup vs baseline: 1.0109x; 1.0058x over previous
.LBB1_89:
	s_andn2_b64 vcc, exec, s[20:21]
	s_cbranch_vccnz .LBB1_102
	v_lshrrev_b32_e32 v1, 6, v0
	v_lshl_or_b32 v1, s33, 3, v1
	v_cmp_gt_i32_e32 vcc, s31, v1
	s_and_saveexec_b64 s[4:5], vcc
	s_cbranch_execz .LBB1_101
	s_mov_b32 s36, 0
	s_cmpk_ge_i32 s33, 36
	s_addc_u32 s36, s36, 0
	s_cmpk_ge_i32 s33, 108
	s_addc_u32 s36, s36, 0
	s_cmpk_ge_i32 s33, 144
	s_addc_u32 s36, s36, 0
	s_cmpk_ge_i32 s33, 180
	s_addc_u32 s36, s36, 0
	s_cmpk_ge_i32 s33, 216
	s_addc_u32 s36, s36, 0
	s_cmpk_ge_i32 s33, 288
	s_addc_u32 s36, s36, 0
	s_cmpk_ge_i32 s33, 360
	s_addc_u32 s36, s36, 0
	s_mul_i32 s36, s36, 40
	s_load_dwordx8 s[40:47], s[24:25], s36
	s_load_dword s48, s[24:25], s36 offset:0x20
	s_waitcnt lgkmcnt(0)
	v_mov_b32_e32 v6, s40
	v_mov_b32_e32 v7, s41
	v_mov_b32_e32 v2, s42
	v_mov_b32_e32 v3, s43
	v_mov_b32_e32 v19, s44
	v_mov_b32_e32 v4, s45
	v_mov_b32_e32 v5, s46
	v_mov_b32_e32 v20, s48
	s_branch .Lprep_frag_go
	s_add_u32 s6, s24, 8
	s_addc_u32 s7, s25, 0
	s_add_u32 s18, s24, 16
	s_addc_u32 s19, s25, 0
	s_add_u32 s20, s24, 20
	s_addc_u32 s21, s25, 0
	s_add_u32 s22, s24, 24
	s_addc_u32 s23, s25, 0
	s_load_dword s15, s[24:25], 0x140
	s_load_dword s28, s[24:25], 0x20
	s_load_dword s14, s[24:25], 0x48
	s_load_dword s13, s[24:25], 0x70
	s_load_dword s12, s[24:25], 0x98
	s_load_dword s11, s[24:25], 0xc0
	s_load_dword s10, s[24:25], 0xe8
	s_load_dword s9, s[24:25], 0x110
	s_load_dword s8, s[24:25], 0x138
	s_waitcnt lgkmcnt(0)
	s_cmp_gt_i32 s15, 1
	s_cselect_b64 s[26:27], -1, 0
	v_cmp_le_i32_e32 vcc, s14, v1
	s_and_b64 s[26:27], s[26:27], vcc
	v_cndmask_b32_e64 v2, 0, 1, s[26:27]
	s_cmp_gt_i32 s15, 2
	v_cmp_gt_i32_e32 vcc, s13, v1
	v_mov_b64_e32 v[8:9], s[22:23]
	v_mov_b32_e32 v20, s28
	v_cndmask_b32_e32 v3, 2, v2, vcc
	s_cselect_b64 vcc, -1, 0
	v_cndmask_b32_e32 v2, v2, v3, vcc
	s_cmp_gt_i32 s15, 3
	v_cmp_gt_i32_e32 vcc, s12, v1
	v_mov_b64_e32 v[12:13], s[20:21]
	v_mov_b64_e32 v[10:11], s[18:19]
	v_cndmask_b32_e32 v3, 3, v2, vcc
	s_cselect_b64 vcc, -1, 0
	v_cndmask_b32_e32 v2, v2, v3, vcc
	s_cmp_gt_i32 s15, 4
	v_cmp_gt_i32_e32 vcc, s11, v1
	v_mov_b64_e32 v[16:17], s[6:7]
	v_mov_b64_e32 v[14:15], s[24:25]
	v_cndmask_b32_e32 v3, 4, v2, vcc
	s_cselect_b64 vcc, -1, 0
	v_cndmask_b32_e32 v2, v2, v3, vcc
	s_cmp_gt_i32 s15, 5
	v_cmp_gt_i32_e32 vcc, s10, v1
	s_nop 1
	v_cndmask_b32_e32 v3, 5, v2, vcc
	s_cselect_b64 vcc, -1, 0
	v_cndmask_b32_e32 v2, v2, v3, vcc
	s_cmp_gt_i32 s15, 6
	v_cmp_gt_i32_e32 vcc, s9, v1
	s_nop 1
	v_cndmask_b32_e32 v3, 6, v2, vcc
	s_cselect_b64 vcc, -1, 0
	v_cndmask_b32_e32 v2, v2, v3, vcc
	s_cmp_gt_i32 s15, 7
	v_cmp_gt_i32_e32 vcc, s8, v1
	s_nop 1
	v_cndmask_b32_e32 v3, 7, v2, vcc
	s_cselect_b64 vcc, -1, 0
	v_cndmask_b32_e32 v18, v2, v3, vcc
	v_cmp_eq_u32_e32 vcc, 1, v18
	s_and_saveexec_b64 s[6:7], vcc
	s_cbranch_execz .LBB1_93
	s_add_u32 s18, s24, 64
	s_addc_u32 s19, s25, 0
	s_add_u32 s20, s24, 60
	s_addc_u32 s21, s25, 0
	s_add_u32 s22, s24, 56
	s_addc_u32 s23, s25, 0
	s_add_u32 s26, s24, 48
	s_addc_u32 s27, s25, 0
	s_add_u32 s28, s24, 40
	s_addc_u32 s29, s25, 0
	v_mov_b64_e32 v[8:9], s[18:19]
	v_mov_b32_e32 v20, s14
	v_mov_b64_e32 v[12:13], s[20:21]
	v_mov_b64_e32 v[10:11], s[22:23]
	v_mov_b64_e32 v[16:17], s[26:27]
	v_mov_b64_e32 v[14:15], s[28:29]

.Lprep_frag_go:
	v_sub_u32_e32 v8, 0, v4
	v_max_i32_e32 v8, v4, v8
	v_cvt_f32_u32_e32 v9, v8
	v_sub_u32_e32 v12, 0, v8
	v_sub_u32_e32 v1, v1, v20
	v_sub_u32_e32 v11, 0, v1
	v_rcp_iflag_f32_e32 v9, v9
	v_max_i32_e32 v11, v1, v11
	v_xor_b32_e32 v10, v1, v4
	v_ashrrev_i32_e32 v10, 31, v10
	v_mul_f32_e32 v9, 0x4f7ffffe, v9
	v_cvt_u32_f32_e32 v9, v9
	v_mul_lo_u32 v12, v12, v9
	v_mul_hi_u32 v12, v9, v12
	v_add_u32_e32 v9, v9, v12
	v_mul_hi_u32 v9, v11, v9
	v_mul_lo_u32 v12, v9, v8
	v_sub_u32_e32 v11, v11, v12
	v_add_u32_e32 v13, 1, v9
	v_cmp_ge_u32_e32 vcc, v11, v8
	v_sub_u32_e32 v12, v11, v8
	s_nop 0
	v_cndmask_b32_e32 v9, v9, v13, vcc
	v_cndmask_b32_e32 v11, v11, v12, vcc
	v_add_u32_e32 v12, 1, v9
	v_cmp_ge_u32_e32 vcc, v11, v8
	s_nop 1
	v_cndmask_b32_e32 v8, v9, v12, vcc
	v_xor_b32_e32 v8, v8, v10
	v_sub_u32_e32 v9, v8, v10
	v_mul_lo_u32 v8, v9, v4
	v_lshrrev_b32_e32 v10, 1, v0
	v_sub_u32_e32 v8, v1, v8
	v_and_b32_e32 v10, 24, v10
	v_lshl_or_b32 v18, v8, 5, v10
	v_lshlrev_b32_e32 v10, 4, v9
	v_and_b32_e32 v1, 15, v0
	v_ashrrev_i32_e32 v11, 31, v10
	v_lshl_add_u64 v[6:7], v[10:11], 2, v[6:7]
	v_lshlrev_b32_e32 v10, 2, v1
	v_or_b32_e32 v1, 1, v18
	v_mad_i64_i32 v[14:15], s[6:7], v1, v19, 0
	v_or_b32_e32 v1, 2, v18
	v_mad_i64_i32 v[16:17], s[6:7], v1, v19, 0
	v_or_b32_e32 v1, 3, v18
	v_mad_i64_i32 v[20:21], s[6:7], v1, v19, 0
	v_or_b32_e32 v1, 4, v18
	v_mad_i64_i32 v[22:23], s[6:7], v1, v19, 0
	v_or_b32_e32 v1, 5, v18
	v_mov_b32_e32 v11, 0
	v_mad_i64_i32 v[24:25], s[6:7], v1, v19, 0
	v_or_b32_e32 v1, 6, v18
	v_lshl_add_u64 v[6:7], v[6:7], 0, v[10:11]
	v_mad_i64_i32 v[12:13], s[6:7], v18, v19, 0
	v_mad_i64_i32 v[26:27], s[6:7], v1, v19, 0
	v_or_b32_e32 v1, 7, v18
	v_lshl_add_u64 v[12:13], v[12:13], 2, v[6:7]
	v_mad_i64_i32 v[18:19], s[6:7], v1, v19, 0
	v_lshl_add_u64 v[14:15], v[14:15], 2, v[6:7]
	v_lshl_add_u64 v[16:17], v[16:17], 2, v[6:7]
	v_lshl_add_u64 v[20:21], v[20:21], 2, v[6:7]
	v_lshl_add_u64 v[22:23], v[22:23], 2, v[6:7]
	v_lshl_add_u64 v[24:25], v[24:25], 2, v[6:7]
	v_lshl_add_u64 v[26:27], v[26:27], 2, v[6:7]
	v_lshl_add_u64 v[6:7], v[18:19], 2, v[6:7]
	global_load_dword v1, v[12:13], off
	global_load_dword v18, v[14:15], off
	global_load_dword v19, v[16:17], off
	global_load_dword v28, v[20:21], off
	global_load_dword v29, v[22:23], off
	global_load_dword v30, v[24:25], off
	global_load_dword v31, v[26:27], off
	global_load_dword v32, v[6:7], off
	s_waitcnt vmcnt(8)
	v_add_u32_e32 v5, v9, v5
	v_mad_u64_u32 v[4:5], s[6:7], v5, v4, v[8:9]
	v_ashrrev_i32_e32 v5, 31, v4
	v_lshlrev_b32_e32 v6, 4, v0
	v_lshlrev_b64 v[4:5], 10, v[4:5]
	v_and_b32_e32 v10, 0x3f0, v6
	v_lshl_add_u64 v[6:7], v[2:3], 0, v[4:5]
	v_lshl_add_u64 v[6:7], v[6:7], 0, v[10:11]
	s_waitcnt vmcnt(6)
	v_cvt_pk_bf16_f32 v2, v1, v18
	s_waitcnt vmcnt(4)
	v_cvt_pk_bf16_f32 v3, v19, v28
	s_waitcnt vmcnt(2)
	v_cvt_pk_bf16_f32 v4, v29, v30
	s_waitcnt vmcnt(0)
	v_cvt_pk_bf16_f32 v5, v31, v32
	global_store_dwordx4 v[6:7], v[2:5], off

.LBB1_103:
	s_andn2_b64 vcc, exec, s[20:21]
	s_cbranch_vccnz .LBB1_116
	v_lshl_or_b32 v1, s30, 9, v0
	v_cmp_gt_i32_e32 vcc, s3, v1
	s_and_saveexec_b64 s[18:19], vcc
	s_cbranch_execz .LBB1_115
	s_mov_b32 s36, 0
	s_cmpk_ge_i32 s30, 108
	s_addc_u32 s36, s36, 0
	s_cmpk_ge_i32 s30, 144
	s_addc_u32 s36, s36, 0
	s_cmpk_ge_i32 s30, 180
	s_addc_u32 s36, s36, 0
	s_cmpk_ge_i32 s30, 216
	s_addc_u32 s36, s36, 0
	s_cmpk_ge_i32 s30, 252
	s_addc_u32 s36, s36, 0
	s_cmpk_ge_i32 s30, 288
	s_addc_u32 s36, s36, 0
	s_cmpk_ge_i32 s30, 324
	s_addc_u32 s36, s36, 0
	s_lshl_b32 s36, s36, 5
	s_load_dwordx8 s[40:47], s[34:35], s36
	s_waitcnt lgkmcnt(0)
	v_mov_b32_e32 v6, s40
	v_mov_b32_e32 v7, s41
	v_mov_b32_e32 v2, s42
	v_mov_b32_e32 v3, s43
	v_mov_b32_e32 v4, s44
	v_mov_b32_e32 v5, s45
	v_mov_b32_e32 v17, s46
	s_branch .Lprep_tr_go
	s_add_u32 s36, s34, 8
	s_addc_u32 s37, s35, 0
	s_add_u32 s38, s34, 16
	s_addc_u32 s39, s35, 0
	s_add_u32 s40, s34, 20
	s_load_dword s33, s[34:35], 0x18
	s_load_dword s3, s[34:35], 0x38
	s_load_dwordx4 s[28:31], s[34:35], 0x50
	s_load_dwordx4 s[4:7], s[34:35], 0xf0
	s_addc_u32 s41, s35, 0
	s_waitcnt lgkmcnt(0)
	s_load_dword s7, s[34:35], 0x100
	s_load_dwordx4 s[24:27], s[34:35], 0x70
	s_load_dwordx4 s[20:23], s[34:35], 0x90
	s_load_dwordx4 s[12:15], s[34:35], 0xb0
	s_load_dwordx4 s[8:11], s[34:35], 0xd0
	s_waitcnt lgkmcnt(0)
	s_cmp_gt_i32 s7, 1
	s_cselect_b64 s[42:43], -1, 0
	v_cmp_le_i32_e32 vcc, s3, v1
	s_and_b64 s[42:43], s[42:43], vcc
	v_cndmask_b32_e64 v2, 0, 1, s[42:43]
	s_cmp_gt_i32 s7, 2
	v_cmp_gt_i32_e32 vcc, s30, v1
	v_mov_b64_e32 v[8:9], s[38:39]
	v_mov_b64_e32 v[10:11], s[40:41]
	v_cndmask_b32_e32 v3, 2, v2, vcc
	s_cselect_b64 vcc, -1, 0
	v_cndmask_b32_e32 v2, v2, v3, vcc
	s_cmp_gt_i32 s7, 3
	v_cmp_gt_i32_e32 vcc, s26, v1
	v_mov_b32_e32 v17, s33
	v_mov_b64_e32 v[12:13], s[36:37]
	v_cndmask_b32_e32 v3, 3, v2, vcc
	s_cselect_b64 vcc, -1, 0
	v_cndmask_b32_e32 v2, v2, v3, vcc
	s_cmp_gt_i32 s7, 4
	v_cmp_gt_i32_e32 vcc, s22, v1
	v_mov_b64_e32 v[14:15], s[34:35]
	s_nop 0
	v_cndmask_b32_e32 v3, 4, v2, vcc
	s_cselect_b64 vcc, -1, 0
	v_cndmask_b32_e32 v2, v2, v3, vcc
	s_cmp_gt_i32 s7, 5
	v_cmp_gt_i32_e32 vcc, s14, v1
	s_nop 1
	v_cndmask_b32_e32 v3, 5, v2, vcc
	s_cselect_b64 vcc, -1, 0
	v_cndmask_b32_e32 v2, v2, v3, vcc
	s_cmp_gt_i32 s7, 6
	v_cmp_gt_i32_e32 vcc, s10, v1
	s_nop 1
	v_cndmask_b32_e32 v3, 6, v2, vcc
	s_cselect_b64 vcc, -1, 0
	v_cndmask_b32_e32 v2, v2, v3, vcc
	s_cmp_gt_i32 s7, 7
	v_cmp_gt_i32_e32 vcc, s6, v1
	s_nop 1
	v_cndmask_b32_e32 v3, 7, v2, vcc
	s_cselect_b64 vcc, -1, 0
	v_cndmask_b32_e32 v16, v2, v3, vcc
	v_cmp_eq_u32_e32 vcc, 1, v16
	s_and_saveexec_b64 s[36:37], vcc
	s_cbranch_execz .LBB1_107
	s_add_u32 s38, s34, 52
	s_addc_u32 s39, s35, 0
	s_add_u32 s40, s34, 48
	s_addc_u32 s41, s35, 0
	s_add_u32 s42, s34, 40
	s_addc_u32 s43, s35, 0
	s_add_u32 s44, s34, 32
	s_addc_u32 s45, s35, 0
	v_mov_b64_e32 v[8:9], s[40:41]
	v_mov_b64_e32 v[10:11], s[38:39]
	v_mov_b32_e32 v17, s3
	v_mov_b64_e32 v[12:13], s[42:43]
	v_mov_b64_e32 v[14:15], s[44:45]

.Lprep_tr_go:
	v_sub_u32_e32 v8, 0, v4
	v_max_i32_e32 v8, v4, v8
	v_cvt_f32_u32_e32 v9, v8
	v_sub_u32_e32 v12, 0, v8
	v_sub_u32_e32 v1, v1, v17
	v_sub_u32_e32 v11, 0, v1
	v_rcp_iflag_f32_e32 v9, v9
	v_max_i32_e32 v11, v1, v11
	v_xor_b32_e32 v10, v1, v4
	v_ashrrev_i32_e32 v10, 31, v10
	v_mul_f32_e32 v9, 0x4f7ffffe, v9
	v_cvt_u32_f32_e32 v9, v9
	s_movk_i32 s3, 0x300
	v_mul_lo_u32 v12, v12, v9
	v_mul_hi_u32 v12, v9, v12
	v_add_u32_e32 v9, v9, v12
	v_mul_hi_u32 v9, v11, v9
	v_mul_lo_u32 v12, v9, v8
	v_sub_u32_e32 v11, v11, v12
	v_add_u32_e32 v13, 1, v9
	v_cmp_ge_u32_e32 vcc, v11, v8
	v_sub_u32_e32 v12, v11, v8
	s_nop 0
	v_cndmask_b32_e32 v9, v9, v13, vcc
	v_cndmask_b32_e32 v11, v11, v12, vcc
	v_add_u32_e32 v12, 1, v9
	v_cmp_ge_u32_e32 vcc, v11, v8
	s_nop 1
	v_cndmask_b32_e32 v8, v9, v12, vcc
	v_xor_b32_e32 v8, v8, v10
	v_sub_u32_e32 v9, v8, v10
	v_mul_lo_u32 v8, v9, v4
	v_lshlrev_b32_e32 v10, 3, v9
	v_sub_u32_e32 v8, v1, v8
	v_or_b32_e32 v1, 1, v10
	v_mad_i64_i32 v[14:15], s[4:5], v1, v4, 0
	v_or_b32_e32 v1, 2, v10
	v_mad_i64_i32 v[16:17], s[4:5], v1, v4, 0
	v_or_b32_e32 v1, 3, v10
	v_mad_i64_i32 v[18:19], s[4:5], v1, v4, 0
	v_or_b32_e32 v1, 4, v10
	v_mad_i64_i32 v[20:21], s[4:5], v1, v4, 0
	v_or_b32_e32 v1, 5, v10
	v_ashrrev_i32_e32 v9, 31, v8
	v_mad_i64_i32 v[22:23], s[4:5], v1, v4, 0
	v_or_b32_e32 v1, 6, v10
	v_lshl_add_u64 v[6:7], v[8:9], 2, v[6:7]
	v_mad_i64_i32 v[12:13], s[4:5], v10, v4, 0
	v_mad_i64_i32 v[24:25], s[4:5], v1, v4, 0
	v_or_b32_e32 v1, 7, v10
	v_lshl_add_u64 v[12:13], v[12:13], 2, v[6:7]
	v_mad_i64_i32 v[26:27], s[4:5], v1, v4, 0
	v_lshl_add_u64 v[14:15], v[14:15], 2, v[6:7]
	v_lshl_add_u64 v[16:17], v[16:17], 2, v[6:7]
	v_lshl_add_u64 v[18:19], v[18:19], 2, v[6:7]
	v_lshl_add_u64 v[20:21], v[20:21], 2, v[6:7]
	v_lshl_add_u64 v[22:23], v[22:23], 2, v[6:7]
	v_lshl_add_u64 v[24:25], v[24:25], 2, v[6:7]
	v_lshl_add_u64 v[6:7], v[26:27], 2, v[6:7]
	global_load_dword v1, v[12:13], off
	global_load_dword v4, v[14:15], off
	global_load_dword v9, v[16:17], off
	global_load_dword v26, v[18:19], off
	global_load_dword v27, v[20:21], off
	global_load_dword v28, v[22:23], off
	global_load_dword v29, v[24:25], off
	global_load_dword v30, v[6:7], off
	v_add_u32_e32 v5, v8, v5
	v_ashrrev_i32_e32 v11, 31, v10
	v_mad_i64_i32 v[6:7], s[4:5], v5, s3, v[2:3]
	v_lshl_add_u64 v[6:7], v[10:11], 1, v[6:7]
	s_waitcnt vmcnt(6)
	v_cvt_pk_bf16_f32 v2, v1, v4
	s_waitcnt vmcnt(4)
	v_cvt_pk_bf16_f32 v3, v9, v26
	s_waitcnt vmcnt(2)
	v_cvt_pk_bf16_f32 v4, v27, v28
	s_waitcnt vmcnt(0)
	v_cvt_pk_bf16_f32 v5, v29, v30
	global_store_dwordx4 v[6:7], v[2:5], off
